# P0 expert-weight loop: moved hipcc's early vmcnt(9) wait below the second half's load burst (vmcnt(63)), keeps 63 loads in flight during the stall
# speedup vs baseline: 1.0182x; 1.0182x over previous
; #define MOE_LOAD(v, it) do { _Pragma("unroll") for (int i_ = 0; i_ < 64; ++i_) v[i_] = __builtin_nontemporal_load((it).src + (size_t)(2 * i_) * (it).stride); } while (0)
;     ...
;         for (int j = 0; j < nmine; j += 2) {
;             const int it1 = gw + (j + 1) * NGW, it2 = gw + (j + 2) * NGW;
;             ib = moe_item(wg, wu, wd, win, wout, wpn, wpd, F.ws, it1 <= last ? it1 : last, F.lane); MOE_LOAD(vb, ib);
;             MOE_PROC(va, ia);
.LBB0_105:
	s_lshl_b64 s[46:47], s[46:47], 3
	global_load_dword v93, v[16:17], off nt
	v_lshl_add_u64 v[16:17], v[16:17], 0, s[46:47]
	v_lshl_add_u64 v[94:95], v[16:17], 0, s[46:47]
	v_lshl_add_u64 v[96:97], v[94:95], 0, s[46:47]
	v_lshl_add_u64 v[102:103], v[96:97], 0, s[46:47]
	v_lshl_add_u64 v[104:105], v[102:103], 0, s[46:47]
	v_lshl_add_u64 v[106:107], v[104:105], 0, s[46:47]
	v_lshl_add_u64 v[108:109], v[106:107], 0, s[46:47]
	v_lshl_add_u64 v[110:111], v[108:109], 0, s[46:47]
	global_load_dword v101, v[16:17], off nt
	global_load_dword v99, v[94:95], off nt
	global_load_dword v100, v[96:97], off nt
	s_nop 0
	global_load_dword v97, v[102:103], off nt
	global_load_dword v98, v[104:105], off nt
	global_load_dword v95, v[106:107], off nt
	global_load_dword v96, v[108:109], off nt
	global_load_dword v94, v[110:111], off nt
	v_lshl_add_u64 v[16:17], v[110:111], 0, s[46:47]
	v_lshl_add_u64 v[102:103], v[16:17], 0, s[46:47]
	global_load_dword v124, v[16:17], off nt
	global_load_dword v104, v[102:103], off nt
	v_lshl_add_u64 v[16:17], v[102:103], 0, s[46:47]
	global_load_dword v114, v[16:17], off nt
	v_lshl_add_u64 v[16:17], v[16:17], 0, s[46:47]
	global_load_dword v105, v[16:17], off nt
	v_lshl_add_u64 v[16:17], v[16:17], 0, s[46:47]
	global_load_dword v115, v[16:17], off nt
	v_lshl_add_u64 v[16:17], v[16:17], 0, s[46:47]
	global_load_dword v106, v[16:17], off nt
	v_lshl_add_u64 v[16:17], v[16:17], 0, s[46:47]
	global_load_dword v116, v[16:17], off nt
	v_lshl_add_u64 v[16:17], v[16:17], 0, s[46:47]
	global_load_dword v107, v[16:17], off nt
	v_lshl_add_u64 v[16:17], v[16:17], 0, s[46:47]
	global_load_dword v117, v[16:17], off nt
	v_lshl_add_u64 v[16:17], v[16:17], 0, s[46:47]
	global_load_dword v108, v[16:17], off nt
	v_lshl_add_u64 v[16:17], v[16:17], 0, s[46:47]
	global_load_dword v118, v[16:17], off nt
	v_lshl_add_u64 v[16:17], v[16:17], 0, s[46:47]
	global_load_dword v109, v[16:17], off nt
	v_lshl_add_u64 v[16:17], v[16:17], 0, s[46:47]
	global_load_dword v119, v[16:17], off nt
	v_lshl_add_u64 v[16:17], v[16:17], 0, s[46:47]
	global_load_dword v110, v[16:17], off nt
	v_lshl_add_u64 v[16:17], v[16:17], 0, s[46:47]
	global_load_dword v120, v[16:17], off nt
	v_lshl_add_u64 v[16:17], v[16:17], 0, s[46:47]
	global_load_dword v111, v[16:17], off nt
	v_lshl_add_u64 v[16:17], v[16:17], 0, s[46:47]
	global_load_dword v121, v[16:17], off nt
	v_lshl_add_u64 v[16:17], v[16:17], 0, s[46:47]
	global_load_dword v112, v[16:17], off nt
	v_lshl_add_u64 v[16:17], v[16:17], 0, s[46:47]
	global_load_dword v122, v[16:17], off nt
	v_lshl_add_u64 v[16:17], v[16:17], 0, s[46:47]
	global_load_dword v102, v[16:17], off nt
	v_lshl_add_u64 v[16:17], v[16:17], 0, s[46:47]
	global_load_dword v103, v[16:17], off nt
	v_lshl_add_u64 v[16:17], v[16:17], 0, s[46:47]
	global_load_dword v113, v[16:17], off nt
	v_lshl_add_u64 v[16:17], v[16:17], 0, s[46:47]
	global_load_dword v123, v[16:17], off nt
	v_lshl_add_u64 v[16:17], v[16:17], 0, s[46:47]
	global_load_dword v125, v[16:17], off nt
	v_lshl_add_u64 v[16:17], v[16:17], 0, s[46:47]
	global_load_dword v126, v[16:17], off nt
	v_lshl_add_u64 v[16:17], v[16:17], 0, s[46:47]
	global_load_dword v127, v[16:17], off nt
	v_lshl_add_u64 v[16:17], v[16:17], 0, s[46:47]
	global_load_dword v128, v[16:17], off nt
	v_lshl_add_u64 v[16:17], v[16:17], 0, s[46:47]
	global_load_dword v129, v[16:17], off nt
	v_lshl_add_u64 v[16:17], v[16:17], 0, s[46:47]
	global_load_dword v130, v[16:17], off nt
	v_lshl_add_u64 v[16:17], v[16:17], 0, s[46:47]
	global_load_dword v131, v[16:17], off nt
	v_lshl_add_u64 v[16:17], v[16:17], 0, s[46:47]
	global_load_dword v132, v[16:17], off nt
	v_lshl_add_u64 v[16:17], v[16:17], 0, s[46:47]
	global_load_dword v133, v[16:17], off nt
	v_lshl_add_u64 v[16:17], v[16:17], 0, s[46:47]
	global_load_dword v134, v[16:17], off nt
	v_lshl_add_u64 v[16:17], v[16:17], 0, s[46:47]
	global_load_dword v135, v[16:17], off nt
	v_lshl_add_u64 v[16:17], v[16:17], 0, s[46:47]
	global_load_dword v136, v[16:17], off nt
	v_lshl_add_u64 v[16:17], v[16:17], 0, s[46:47]
	global_load_dword v137, v[16:17], off nt
	v_lshl_add_u64 v[16:17], v[16:17], 0, s[46:47]
	global_load_dword v138, v[16:17], off nt
	v_lshl_add_u64 v[16:17], v[16:17], 0, s[46:47]
	global_load_dword v139, v[16:17], off nt
	v_lshl_add_u64 v[16:17], v[16:17], 0, s[46:47]
	global_load_dword v140, v[16:17], off nt
	v_lshl_add_u64 v[16:17], v[16:17], 0, s[46:47]
	global_load_dword v141, v[16:17], off nt
	v_lshl_add_u64 v[16:17], v[16:17], 0, s[46:47]
	global_load_dword v142, v[16:17], off nt
	v_lshl_add_u64 v[16:17], v[16:17], 0, s[46:47]
	global_load_dword v143, v[16:17], off nt
	v_lshl_add_u64 v[16:17], v[16:17], 0, s[46:47]
	global_load_dword v144, v[16:17], off nt
	v_lshl_add_u64 v[16:17], v[16:17], 0, s[46:47]
	global_load_dword v146, v[16:17], off nt
	v_lshl_add_u64 v[16:17], v[16:17], 0, s[46:47]
	global_load_dword v147, v[16:17], off nt
	v_lshl_add_u64 v[16:17], v[16:17], 0, s[46:47]
	global_load_dword v148, v[16:17], off nt
	v_lshl_add_u64 v[16:17], v[16:17], 0, s[46:47]
	global_load_dword v149, v[16:17], off nt
	v_lshl_add_u64 v[16:17], v[16:17], 0, s[46:47]
	global_load_dword v151, v[16:17], off nt
	v_lshl_add_u64 v[16:17], v[16:17], 0, s[46:47]
	global_load_dword v152, v[16:17], off nt
	v_lshl_add_u64 v[16:17], v[16:17], 0, s[46:47]
	global_load_dword v153, v[16:17], off nt
	v_lshl_add_u64 v[16:17], v[16:17], 0, s[46:47]
	global_load_dword v154, v[16:17], off nt
	v_lshl_add_u64 v[16:17], v[16:17], 0, s[46:47]
	global_load_dword v155, v[16:17], off nt
	v_lshl_add_u64 v[16:17], v[16:17], 0, s[46:47]
	global_load_dword v157, v[16:17], off nt
	v_lshl_add_u64 v[16:17], v[16:17], 0, s[46:47]
	global_load_dword v158, v[16:17], off nt
	v_lshl_add_u64 v[16:17], v[16:17], 0, s[46:47]
	s_waitcnt vmcnt(63)
	ds_write2st64_b32 v28, v87, v92 offset1:1
	ds_write2st64_b32 v28, v91, v90 offset0:2 offset1:3
	ds_write2st64_b32 v28, v89, v88 offset0:4 offset1:5
	ds_write2st64_b32 v28, v86, v85 offset0:6 offset1:7
	ds_write2st64_b32 v21, v83, v84 offset0:8 offset1:9
	ds_write2st64_b32 v21, v79, v80 offset0:10 offset1:11
	ds_write2st64_b32 v21, v75, v76 offset0:12 offset1:13
	ds_write2st64_b32 v21, v71, v72 offset0:14 offset1:15
	ds_write2st64_b32 v22, v65, v66 offset0:16 offset1:17
	ds_write2st64_b32 v22, v61, v62 offset0:18 offset1:19
	ds_write2st64_b32 v22, v57, v58 offset0:20 offset1:21
	ds_write2st64_b32 v22, v53, v54 offset0:22 offset1:23
	ds_write2st64_b32 v23, v45, v46 offset0:24 offset1:25
	ds_write2st64_b32 v23, v35, v36 offset0:26 offset1:27
	ds_write2st64_b32 v23, v33, v34 offset0:28 offset1:29
	ds_write2st64_b32 v23, v31, v32 offset0:30 offset1:31
	ds_write2st64_b32 v24, v29, v30 offset0:32 offset1:33
	ds_write2st64_b32 v24, v81, v82 offset0:34 offset1:35
	ds_write2st64_b32 v24, v77, v78 offset0:36 offset1:37
	ds_write2st64_b32 v24, v73, v74 offset0:38 offset1:39
	ds_write2st64_b32 v25, v69, v70 offset0:40 offset1:41
	ds_write2st64_b32 v25, v67, v68 offset0:42 offset1:43
	ds_write2st64_b32 v25, v63, v64 offset0:44 offset1:45
	ds_write2st64_b32 v25, v59, v60 offset0:46 offset1:47
	ds_write2st64_b32 v26, v55, v56 offset0:48 offset1:49
	ds_write2st64_b32 v26, v51, v52 offset0:50 offset1:51
	global_load_dword v159, v[16:17], off nt
	ds_write2st64_b32 v26, v38, v39 offset0:52 offset1:53
	ds_write2st64_b32 v26, v40, v42 offset0:54 offset1:55
	ds_write2st64_b32 v27, v37, v41 offset0:56 offset1:57
	ds_write2st64_b32 v27, v43, v44 offset0:58 offset1:59
	ds_write2st64_b32 v27, v47, v48 offset0:60 offset1:61
	ds_write2st64_b32 v27, v49, v50 offset0:62 offset1:63
	s_waitcnt lgkmcnt(0)
	ds_read2_b32 v[16:17], v1 offset1:32
	v_mov_b32_e32 v30, 0
	ds_read2_b32 v[32:33], v1 offset0:128 offset1:160
	v_mov_b32_e32 v31, 0
	v_add_u32_e32 v145, 0x400, v1
	s_waitcnt lgkmcnt(1)
	v_mul_f32_e32 v4, 0x42800000, v16
	v_mul_f32_e32 v15, 0x42800000, v17
	ds_read2_b32 v[16:17], v1 offset0:64 offset1:96
	v_cvt_pk_fp8_f32 v30, v4, v15
	ds_read2_b32 v[34:35], v145 offset0:128 offset1:160
	v_add_u32_e32 v150, 0x400, v9
	ds_read2_b32 v[38:39], v150 offset0:128 offset1:160
	s_waitcnt lgkmcnt(2)
	v_mul_f32_e32 v4, 0x42800000, v16
	v_mul_f32_e32 v15, 0x42800000, v17
	ds_read2_b32 v[16:17], v1 offset0:192 offset1:224
	v_cvt_pk_fp8_f32 v30, v4, v15 op_sel:[0,0,1]
	v_mul_f32_e32 v4, 0x42800000, v32
	v_mul_f32_e32 v15, 0x42800000, v33
	v_cvt_pk_fp8_f32 v31, v4, v15
	s_waitcnt lgkmcnt(0)
	v_mul_f32_e32 v4, 0x42800000, v16
	v_mul_f32_e32 v15, 0x42800000, v17
	ds_read2_b32 v[16:17], v145 offset0:64 offset1:96
	ds_read2_b32 v[32:33], v145 offset1:32
	v_cvt_pk_fp8_f32 v31, v4, v15 op_sel:[0,0,1]
	v_lshl_add_u64 v[10:11], v[10:11], 0, v[6:7]
	v_add_u32_e32 v156, 0x400, v18
	s_waitcnt lgkmcnt(1)
	v_mul_f32_e32 v29, 0x42800000, v16
	v_mul_f32_e32 v36, 0x42800000, v17
	ds_read2_b32 v[16:17], v145 offset0:192 offset1:224
	s_waitcnt lgkmcnt(1)
	v_mul_f32_e32 v4, 0x42800000, v32
	v_mul_f32_e32 v15, 0x42800000, v33
	v_mov_b32_e32 v32, 0
	v_cvt_pk_fp8_f32 v32, v4, v15
	v_mul_f32_e32 v4, 0x42800000, v34
	v_mul_f32_e32 v15, 0x42800000, v35
	v_mov_b32_e32 v33, 0
	ds_read2_b32 v[34:35], v9 offset1:32
	v_cvt_pk_fp8_f32 v33, v4, v15
	s_waitcnt lgkmcnt(1)
	v_mul_f32_e32 v4, 0x42800000, v16
	v_mul_f32_e32 v15, 0x42800000, v17
	ds_read2_b32 v[16:17], v9 offset0:64 offset1:96
	v_cvt_pk_fp8_f32 v32, v29, v36 op_sel:[0,0,1]
	ds_read2_b32 v[36:37], v9 offset0:128 offset1:160
	v_cvt_pk_fp8_f32 v33, v4, v15 op_sel:[0,0,1]
	s_waitcnt lgkmcnt(2)
	v_mul_f32_e32 v4, 0x42800000, v34
	v_mul_f32_e32 v15, 0x42800000, v35
	v_mov_b32_e32 v34, 0
	v_cvt_pk_fp8_f32 v34, v4, v15
	s_waitcnt lgkmcnt(1)
	v_mul_f32_e32 v4, 0x42800000, v16
	v_mul_f32_e32 v15, 0x42800000, v17
	ds_read2_b32 v[16:17], v9 offset0:192 offset1:224
	s_waitcnt lgkmcnt(1)
	v_mul_f32_e32 v29, 0x42800000, v36
	v_mul_f32_e32 v36, 0x42800000, v37
	v_mov_b32_e32 v35, 0
	v_cvt_pk_fp8_f32 v35, v29, v36
	ds_read2_b32 v[36:37], v150 offset1:32
	v_cvt_pk_fp8_f32 v34, v4, v15 op_sel:[0,0,1]
	s_waitcnt lgkmcnt(1)
	v_mul_f32_e32 v4, 0x42800000, v16
	v_mul_f32_e32 v15, 0x42800000, v17
	ds_read2_b32 v[16:17], v150 offset0:64 offset1:96
	v_cvt_pk_fp8_f32 v35, v4, v15 op_sel:[0,0,1]
	s_waitcnt lgkmcnt(1)
	v_mul_f32_e32 v4, 0x42800000, v36
	v_mul_f32_e32 v15, 0x42800000, v37
	v_mov_b32_e32 v36, 0
	v_cvt_pk_fp8_f32 v36, v4, v15
	s_waitcnt lgkmcnt(0)
	v_mul_f32_e32 v4, 0x42800000, v16
	v_mul_f32_e32 v15, 0x42800000, v17
	ds_read2_b32 v[16:17], v150 offset0:192 offset1:224
	v_cvt_pk_fp8_f32 v36, v4, v15 op_sel:[0,0,1]
	v_mul_f32_e32 v4, 0x42800000, v38
	v_mul_f32_e32 v15, 0x42800000, v39
	v_mov_b32_e32 v37, 0
	v_cvt_pk_fp8_f32 v37, v4, v15
	s_waitcnt lgkmcnt(0)
; __device__ __forceinline__ MoeItem moe_item(const float* wg, const float* wu, const float* wd, const float* win, const float* wout, const float* wpn, const float* wpd, unsigned char* ws, int r, int lane) {
;     ...
;     const int mat = r / MOE_IE, q = r % MOE_IE, e = mat / 3, which = mat % 3, kb = q / 64, nb = q % 64, n0 = nb * 32;
;     const float* src = (which == 0 ? wg : (which == 1 ? wu : wd)) + (size_t)e * DM * DFF + (size_t)(kb * 128 + (lane >> 5)) * DFF + n0 + (lane & 31);
;     unsigned char* dst;
;     if (which < 2) dst = ws + WS_WGUT + ((size_t)(e * 16 + (n0 >> 7)) * 256 + which * 128 + (n0 & 127)) * DM;
;     else dst = ws + WS_WDT + ((size_t)e * DM + n0) * DFF;
;     MoeItem it; it.stride = DFF; it.dpitch = DM; it.src = src; it.dst = dst + kb * 128 + (size_t)(lane >> 3) * DM + 16 * (lane & 7); return it;
	v_mul_f32_e32 v4, 0x42800000, v16
	v_mul_f32_e32 v15, 0x42800000, v17
	ds_read2_b32 v[16:17], v18 offset1:32
	v_cvt_pk_fp8_f32 v37, v4, v15 op_sel:[0,0,1]
	global_store_dwordx4 v[10:11], v[30:33], off
	ds_read2_b32 v[32:33], v18 offset0:64 offset1:96
	s_lshl_b64 s[38:39], s[38:39], 3
	s_waitcnt lgkmcnt(1)
	v_mul_f32_e32 v4, 0x42800000, v16
	v_mul_f32_e32 v15, 0x42800000, v17
	ds_read2_b32 v[16:17], v18 offset0:128 offset1:160
	v_mov_b32_e32 v30, 0
	v_cvt_pk_fp8_f32 v30, v4, v15
	s_waitcnt lgkmcnt(1)
	v_mul_f32_e32 v4, 0x42800000, v32
	v_mov_b32_e32 v31, 0
	s_waitcnt lgkmcnt(0)
	v_mul_f32_e32 v29, 0x42800000, v16
	v_mul_f32_e32 v32, 0x42800000, v17
	ds_read2_b32 v[16:17], v18 offset0:192 offset1:224
	v_mul_f32_e32 v15, 0x42800000, v33
	v_cvt_pk_fp8_f32 v31, v29, v32
	ds_read2_b32 v[32:33], v156 offset1:32
	v_cvt_pk_fp8_f32 v30, v4, v15 op_sel:[0,0,1]
	s_waitcnt lgkmcnt(1)
	v_mul_f32_e32 v4, 0x42800000, v16
	v_mul_f32_e32 v15, 0x42800000, v17
	ds_read2_b32 v[16:17], v156 offset0:64 offset1:96
	v_lshl_add_u64 v[10:11], v[10:11], 0, s[38:39]
	global_store_dwordx4 v[10:11], v[34:37], off
	ds_read2_b32 v[34:35], v156 offset0:128 offset1:160
	v_cvt_pk_fp8_f32 v31, v4, v15 op_sel:[0,0,1]
	s_waitcnt lgkmcnt(2)
	v_mul_f32_e32 v4, 0x42800000, v32
	v_mul_f32_e32 v15, 0x42800000, v33
	v_mov_b32_e32 v32, 0
	v_cvt_pk_fp8_f32 v32, v4, v15
	s_waitcnt lgkmcnt(1)
	v_mul_f32_e32 v4, 0x42800000, v16
	v_mul_f32_e32 v15, 0x42800000, v17
	ds_read2_b32 v[16:17], v156 offset0:192 offset1:224
	s_waitcnt lgkmcnt(1)
	v_mul_f32_e32 v29, 0x42800000, v34
	v_mul_f32_e32 v34, 0x42800000, v35
	v_mov_b32_e32 v33, 0
	v_cvt_pk_fp8_f32 v33, v29, v34
	ds_read2_b32 v[34:35], v19 offset1:32
	v_cvt_pk_fp8_f32 v32, v4, v15 op_sel:[0,0,1]
	s_waitcnt lgkmcnt(1)
	v_mul_f32_e32 v4, 0x42800000, v16
	v_mul_f32_e32 v15, 0x42800000, v17
	ds_read2_b32 v[16:17], v19 offset0:64 offset1:96
	ds_read2_b32 v[36:37], v19 offset0:128 offset1:160
	v_cvt_pk_fp8_f32 v33, v4, v15 op_sel:[0,0,1]
	s_waitcnt lgkmcnt(2)
	v_mul_f32_e32 v4, 0x42800000, v34
	v_mul_f32_e32 v15, 0x42800000, v35
	v_mov_b32_e32 v34, 0
	v_cvt_pk_fp8_f32 v34, v4, v15
	s_waitcnt lgkmcnt(1)
	v_mul_f32_e32 v4, 0x42800000, v16
	v_mul_f32_e32 v15, 0x42800000, v17
	ds_read2_b32 v[16:17], v19 offset0:192 offset1:224
	s_waitcnt lgkmcnt(1)
	v_mul_f32_e32 v29, 0x42800000, v36
	v_mul_f32_e32 v36, 0x42800000, v37
	v_mov_b32_e32 v35, 0
	v_add_u32_e32 v160, 0x400, v19
	v_cvt_pk_fp8_f32 v35, v29, v36
	ds_read2_b32 v[36:37], v160 offset1:32
	v_cvt_pk_fp8_f32 v34, v4, v15 op_sel:[0,0,1]
	s_waitcnt lgkmcnt(1)
	v_mul_f32_e32 v4, 0x42800000, v16
	v_mul_f32_e32 v15, 0x42800000, v17
	ds_read2_b32 v[16:17], v160 offset0:64 offset1:96
	ds_read2_b32 v[38:39], v160 offset0:128 offset1:160
	v_cvt_pk_fp8_f32 v35, v4, v15 op_sel:[0,0,1]
	s_waitcnt lgkmcnt(2)
	v_mul_f32_e32 v4, 0x42800000, v36
	v_mul_f32_e32 v15, 0x42800000, v37
	v_mov_b32_e32 v36, 0
	v_cvt_pk_fp8_f32 v36, v4, v15
	s_waitcnt lgkmcnt(1)
	v_mul_f32_e32 v4, 0x42800000, v16
	v_mul_f32_e32 v15, 0x42800000, v17
	ds_read2_b32 v[16:17], v160 offset0:192 offset1:224
	s_waitcnt lgkmcnt(1)
	v_mul_f32_e32 v29, 0x42800000, v38
	v_mul_f32_e32 v38, 0x42800000, v39
	v_mov_b32_e32 v37, 0
	v_cvt_pk_fp8_f32 v37, v29, v38
	v_cvt_pk_fp8_f32 v36, v4, v15 op_sel:[0,0,1]
	s_waitcnt lgkmcnt(0)
	v_mul_f32_e32 v4, 0x42800000, v16
	v_mul_f32_e32 v15, 0x42800000, v17
	v_cvt_pk_fp8_f32 v37, v4, v15 op_sel:[0,0,1]
	v_lshl_add_u64 v[10:11], v[10:11], 0, s[38:39]
	global_store_dwordx4 v[10:11], v[30:33], off
	v_lshl_add_u64 v[10:11], v[10:11], 0, s[38:39]
	global_store_dwordx4 v[10:11], v[34:37], off
	s_waitcnt lgkmcnt(0)
	s_add_i32 s3, s89, s3
	s_min_i32 s43, s3, s7
	s_cmp_lt_i32 s43, 0x19000
	s_mov_b64 s[38:39], -1
	s_cbranch_scc0 .LBB0_126
	s_cmp_lt_i32 s43, 0x18c00
	s_cbranch_scc0 .LBB0_123
	s_cmp_lt_i32 s43, 0x18000
	s_cbranch_scc0 .LBB0_113
	s_ashr_i32 s4, s43, 31
	s_lshr_b32 s4, s4, 22
	s_add_i32 s4, s43, s4
	s_ashr_i32 s39, s4, 10
	s_and_b32 s4, s4, 0xfc00
	s_sub_i32 s46, s43, s4
	s_mul_hi_i32 s4, s43, 0x2aaaaaab
	s_lshr_b32 s38, s4, 31
	s_ashr_i32 s4, s4, 9
	s_add_i32 s38, s4, s38
	s_mul_hi_i32 s4, s39, 0x55555556
	s_lshr_b32 s45, s4, 31
	s_add_i32 s4, s4, s45
	s_mul_i32 s4, s4, 3
	s_sub_i32 s4, s39, s4
	s_sext_i32_i16 s39, s46
	s_bfe_u32 s39, s39, 0x60019
	s_add_i32 s45, s46, s39
	s_and_b32 s39, s45, 0xffc0
	s_sub_i32 s39, s46, s39
	s_sext_i32_i16 s84, s39
	s_lshl_b32 s46, s84, 5
	s_ashr_i32 s39, s38, 31
	s_ashr_i32 s47, s46, 31
	s_cmp_gt_i32 s4, 1
	s_mov_b64 s[70:71], -1
	s_cbranch_scc0 .LBB0_110
	s_lshl_b64 s[68:69], s[38:39], 22
	s_lshl_b64 s[70:71], s[46:47], 11
	s_add_u32 s68, s73, s68
	s_addc_u32 s69, s74, s69
	s_add_u32 s68, s68, s70
	s_addc_u32 s69, s69, s71
	s_mov_b64 s[70:71], 0
